# stack: MFMA-section cleanup + K-loop alignment + barrier publish-before-acquire + retention state loop keeps two tiles in flight + MoE routing gather issues 8 row loads before converting (was 1 at a t
# speedup vs baseline: 1.0107x; 1.0050x over previous
; DI unsigned cvt_pk_bf16(float lo, float hi) { const f32x2_t v = {lo, hi}; return __builtin_bit_cast(unsigned, __builtin_convertvector(v, bf16x2_t)); }
; DI KArgP kargs() { KArgP p = (KArgP)__builtin_amdgcn_kernarg_segment_ptr(); asm volatile("" : "+s"(p)); return p; }
; __global__ void __launch_bounds__(512, 2) mk_fwd(FArgs args) {
;     ...
;         { const size_t n4 = (size_t)DEPTH * NTOK * PLED / 4; const f32x4* s = (const f32x4*)kargs()->in[1]; u32x2* d = (u32x2*)(ws + WS_PBP);
;           for (size_t i = (size_t)bid * 512 + tid; i < n4; i += (size_t)G * 512) { const f32x4 v = s[i]; d[(i >> 6) * (D_ / 4) + (i & 63)] = (u32x2){pg8::cvt_pk_bf16(v.x, v.y), pg8::cvt_pk_bf16(v.z, v.w)}; } }
.LBB0_129:
	s_or_b64 exec, exec, s[8:9]
	s_mov_b64 s[8:9], 0x100000
	s_mov_b64 s[10:11], s[0:1]
	v_cmp_gt_u64_e32 vcc, s[8:9], v[0:1]
	s_and_saveexec_b64 s[8:9], vcc
	s_cbranch_execz .LBB0_132
	s_load_dwordx2 s[14:15], s[10:11], 0x8
	v_lshlrev_b32_e32 v2, 3, v169
	v_mov_b32_e32 v3, 0
	s_waitcnt vmcnt(22)
	v_lshl_add_u64 v[4:5], s[4:5], 0, v[2:3]
	s_mov_b64 s[12:13], 0x2a00000
	s_ashr_i32 s35, s34, 31
	v_lshl_add_u64 v[4:5], v[4:5], 0, s[12:13]
	s_lshl_b64 s[12:13], s[2:3], 12
	s_lshl_b64 s[10:11], s[34:35], 9
	v_lshl_add_u64 v[6:7], v[128:129], 3, s[12:13]
	s_lshl_b64 s[12:13], s[34:35], 12
	s_lshl_b64 s[16:17], s[2:3], 13
	s_waitcnt lgkmcnt(0)
	s_add_u32 s14, s14, s16
	s_addc_u32 s15, s15, s17
	s_waitcnt vmcnt(21)
	v_lshl_add_u64 v[8:9], v[128:129], 4, s[14:15]
	s_lshl_b64 s[14:15], s[34:35], 13
	s_mov_b64 s[16:17], 0
	s_mov_b64 s[18:19], 0xfffff
	s_waitcnt vmcnt(0)
	s_mul_i32 s24, s10, 3
	s_mov_b32 s25, 0
.Lmy_p4:
	v_lshl_add_u64 v[58:59], v[0:1], 0, s[24:25]
	v_cmp_ge_u64_e32 vcc, s[18:19], v[58:59]
	s_cmp_eq_u64 vcc, exec
	s_cbranch_scc0 .Lmy_p4_exit
	v_lshl_add_u64 v[36:37], v[8:9], 0, s[14:15]
	v_lshl_add_u64 v[38:39], v[36:37], 0, s[14:15]
	v_lshl_add_u64 v[40:41], v[38:39], 0, s[14:15]
	global_load_dwordx4 v[20:23], v[8:9], off
	global_load_dwordx4 v[24:27], v[36:37], off
	global_load_dwordx4 v[28:31], v[38:39], off
	global_load_dwordx4 v[32:35], v[40:41], off
	v_lshl_add_u64 v[8:9], v[40:41], 0, s[14:15]
	v_lshl_add_u64 v[0:1], v[58:59], 0, s[10:11]
	v_and_b32_e32 v2, 0x7ffe00, v6
	v_lshlrev_b32_e32 v2, 3, v2
	v_lshl_add_u64 v[6:7], v[6:7], 0, s[12:13]
	v_lshl_add_u64 v[14:15], v[4:5], 0, v[2:3]
	s_waitcnt vmcnt(3)
	v_cvt_pk_bf16_f32 v42, v20, v21
	v_cvt_pk_bf16_f32 v43, v22, v23
	global_store_dwordx2 v[14:15], v[42:43], off
	v_and_b32_e32 v2, 0x7ffe00, v6
	v_lshlrev_b32_e32 v2, 3, v2
	v_lshl_add_u64 v[6:7], v[6:7], 0, s[12:13]
	v_lshl_add_u64 v[14:15], v[4:5], 0, v[2:3]
	s_waitcnt vmcnt(3)
	v_cvt_pk_bf16_f32 v44, v24, v25
	v_cvt_pk_bf16_f32 v45, v26, v27
	global_store_dwordx2 v[14:15], v[44:45], off
	v_and_b32_e32 v2, 0x7ffe00, v6
	v_lshlrev_b32_e32 v2, 3, v2
	v_lshl_add_u64 v[6:7], v[6:7], 0, s[12:13]
	v_lshl_add_u64 v[14:15], v[4:5], 0, v[2:3]
	s_waitcnt vmcnt(3)
	v_cvt_pk_bf16_f32 v46, v28, v29
	v_cvt_pk_bf16_f32 v47, v30, v31
	global_store_dwordx2 v[14:15], v[46:47], off
	v_and_b32_e32 v2, 0x7ffe00, v6
	v_lshlrev_b32_e32 v2, 3, v2
	v_lshl_add_u64 v[6:7], v[6:7], 0, s[12:13]
	v_lshl_add_u64 v[14:15], v[4:5], 0, v[2:3]
	s_waitcnt vmcnt(3)
	v_cvt_pk_bf16_f32 v48, v32, v33
	v_cvt_pk_bf16_f32 v49, v34, v35
	global_store_dwordx2 v[14:15], v[48:49], off
	s_branch .Lmy_p4
.Lmy_p4_exit:
	v_cmp_ge_u64_e32 vcc, s[18:19], v[0:1]
	s_and_b64 exec, exec, vcc
	s_cbranch_execz .LBB0_132

; DI unsigned pk4_fp8(float a, float b, float c, float d) { int w = __builtin_amdgcn_cvt_pk_fp8_f32(sat8(a), sat8(b), 0, false); w = __builtin_amdgcn_cvt_pk_fp8_f32(sat8(c), sat8(d), w, true); return (unsigned)w; }
; template <int l>
; DI void layer_body(LAS unsigned char* lds, const XcdBarrier& bar, const int lo, const int hi, const int G, const int vcu) {
;     ...
;                 for (int r = wave; r < 64; r += 8) { const int dest = dl[r], tk = dl[64 + r];
;                     const u32x4* s = (const u32x4*)(X1B + (size_t)tk * D_); u32x2* d = (u32x2*)((unsigned char*)XS + (size_t)dest * D_);
; #pragma unroll
;                     for (int q = 0; q < 4; ++q) { const u32x4 w = s[lane + 64 * q]; float x[8]; att::unpack8(w, x);
;                         d[lane + 64 * q] = (u32x2){pg8::pk4_fp8(x[0] * X_SC, x[1] * X_SC, x[2] * X_SC, x[3] * X_SC), pg8::pk4_fp8(x[4] * X_SC, x[5] * X_SC, x[6] * X_SC, x[7] * X_SC)}; } }
.LBB0_1539:
	v_mov_b32_e32 v1, s17
	ds_read2st64_b32 v[6:7], v1 offset1:1
	v_add_u32_e32 v1, 32, v1
	ds_read2st64_b32 v[34:35], v1 offset1:1
	v_mov_b32_e32 v18, 0
	v_mov_b32_e32 v19, 0
	s_add_i32 s17, s17, 64
	s_add_i32 s16, s16, 16
	s_waitcnt lgkmcnt(0)
	v_ashrrev_i32_e32 v29, 31, v7
	v_mov_b32_e32 v28, v7
	v_lshlrev_b64 v[30:31], 12, v[28:29]
	v_lshl_add_u64 v[32:33], v[2:3], 0, v[30:31]
	global_load_dwordx4 v[248:251], v[32:33], off
	global_load_dwordx4 v[244:247], v[32:33], off offset:1024
	global_load_dwordx4 v[240:243], v[32:33], off offset:2048
	global_load_dwordx4 v[236:239], v[32:33], off offset:3072
	v_ashrrev_i32_e32 v29, 31, v35
	v_mov_b32_e32 v28, v35
	v_lshlrev_b64 v[30:31], 12, v[28:29]
	v_lshl_add_u64 v[32:33], v[2:3], 0, v[30:31]
	global_load_dwordx4 v[232:235], v[32:33], off
	global_load_dwordx4 v[228:231], v[32:33], off offset:1024
	global_load_dwordx4 v[224:227], v[32:33], off offset:2048
	global_load_dwordx4 v[220:223], v[32:33], off offset:3072
	v_ashrrev_i32_e32 v21, 31, v7
	v_mov_b32_e32 v20, v7
	v_ashrrev_i32_e32 v9, 31, v6
	v_mov_b32_e32 v8, v6
	v_lshlrev_b64 v[6:7], 12, v[20:21]
	v_lshlrev_b64 v[8:9], 11, v[8:9]
	v_lshl_add_u64 v[20:21], v[2:3], 0, v[6:7]
	v_lshl_add_u64 v[22:23], v[4:5], 0, v[8:9]
	s_nop 0
	s_cmp_gt_i32 s16, 55
	s_nop 0
	s_waitcnt vmcnt(7)
	v_lshlrev_b32_e32 v1, 16, v248
	v_and_b32_e32 v6, 0xffff0000, v248
	v_lshlrev_b32_e32 v25, 16, v250
	v_and_b32_e32 v8, 0xffff0000, v250
	v_mul_f32_e32 v1, 0x41800000, v1
	v_mul_f32_e32 v6, 0x41800000, v6
	v_mul_f32_e32 v25, 0x41800000, v25
	v_mul_f32_e32 v8, 0x41800000, v8
	v_med3_f32 v1, v1, s44, v16
	v_med3_f32 v6, v6, s44, v16
	v_med3_f32 v25, v25, s44, v16
	v_med3_f32 v8, v8, s44, v16
	v_cvt_pk_fp8_f32 v18, v1, v6
	v_cvt_pk_fp8_f32 v19, v25, v8
	v_lshlrev_b32_e32 v17, 16, v249
	v_and_b32_e32 v7, 0xffff0000, v249
	v_lshlrev_b32_e32 v26, 16, v251
	v_and_b32_e32 v9, 0xffff0000, v251
	v_mul_f32_e32 v17, 0x41800000, v17
	v_mul_f32_e32 v7, 0x41800000, v7
	v_mul_f32_e32 v26, 0x41800000, v26
	v_mul_f32_e32 v9, 0x41800000, v9
	v_med3_f32 v17, v17, s44, v16
	v_med3_f32 v7, v7, s44, v16
	v_med3_f32 v26, v26, s44, v16
	v_med3_f32 v9, v9, s44, v16
	v_cvt_pk_fp8_f32 v18, v17, v7 op_sel:[0,0,1]
	v_cvt_pk_fp8_f32 v19, v26, v9 op_sel:[0,0,1]
	global_store_dwordx2 v[22:23], v[18:19], off
	s_nop 0
	v_mov_b32_e32 v18, 0
	v_mov_b32_e32 v19, 0
	s_nop 0
	s_waitcnt vmcnt(7)
	v_lshlrev_b32_e32 v1, 16, v244
	v_and_b32_e32 v6, 0xffff0000, v244
	v_lshlrev_b32_e32 v25, 16, v246
	v_and_b32_e32 v8, 0xffff0000, v246
	v_mul_f32_e32 v1, 0x41800000, v1
	v_mul_f32_e32 v6, 0x41800000, v6
	v_mul_f32_e32 v25, 0x41800000, v25
	v_mul_f32_e32 v8, 0x41800000, v8
	v_med3_f32 v1, v1, s44, v16
	v_med3_f32 v6, v6, s44, v16
	v_med3_f32 v25, v25, s44, v16
	v_med3_f32 v8, v8, s44, v16
	v_cvt_pk_fp8_f32 v18, v1, v6
	v_cvt_pk_fp8_f32 v19, v25, v8
	v_lshlrev_b32_e32 v17, 16, v245
	v_and_b32_e32 v7, 0xffff0000, v245
	v_lshlrev_b32_e32 v26, 16, v247
	v_and_b32_e32 v9, 0xffff0000, v247
	v_mul_f32_e32 v17, 0x41800000, v17
	v_mul_f32_e32 v7, 0x41800000, v7
	v_mul_f32_e32 v26, 0x41800000, v26
	v_mul_f32_e32 v9, 0x41800000, v9
	v_med3_f32 v17, v17, s44, v16
	v_med3_f32 v7, v7, s44, v16
	v_med3_f32 v26, v26, s44, v16
	v_med3_f32 v9, v9, s44, v16
	v_cvt_pk_fp8_f32 v18, v17, v7 op_sel:[0,0,1]
	v_cvt_pk_fp8_f32 v19, v26, v9 op_sel:[0,0,1]
	global_store_dwordx2 v[22:23], v[18:19], off offset:512
	s_nop 0
	v_mov_b32_e32 v18, 0
	v_mov_b32_e32 v19, 0
	s_nop 0
	s_waitcnt vmcnt(7)
	v_lshlrev_b32_e32 v1, 16, v240
	v_and_b32_e32 v6, 0xffff0000, v240
	v_lshlrev_b32_e32 v25, 16, v242
	v_and_b32_e32 v8, 0xffff0000, v242
	v_mul_f32_e32 v1, 0x41800000, v1
	v_mul_f32_e32 v6, 0x41800000, v6
	v_mul_f32_e32 v25, 0x41800000, v25
	v_mul_f32_e32 v8, 0x41800000, v8
	v_med3_f32 v1, v1, s44, v16
	v_med3_f32 v6, v6, s44, v16
	v_med3_f32 v25, v25, s44, v16
	v_med3_f32 v8, v8, s44, v16
	v_cvt_pk_fp8_f32 v18, v1, v6
	v_cvt_pk_fp8_f32 v19, v25, v8
	v_lshlrev_b32_e32 v17, 16, v241
	v_and_b32_e32 v7, 0xffff0000, v241
	v_lshlrev_b32_e32 v26, 16, v243
	v_and_b32_e32 v9, 0xffff0000, v243
	v_mul_f32_e32 v17, 0x41800000, v17
	v_mul_f32_e32 v7, 0x41800000, v7
	v_mul_f32_e32 v26, 0x41800000, v26
	v_mul_f32_e32 v9, 0x41800000, v9
	v_med3_f32 v17, v17, s44, v16
	v_med3_f32 v7, v7, s44, v16
	v_med3_f32 v26, v26, s44, v16
	v_med3_f32 v9, v9, s44, v16
	v_cvt_pk_fp8_f32 v18, v17, v7 op_sel:[0,0,1]
	v_cvt_pk_fp8_f32 v19, v26, v9 op_sel:[0,0,1]
	global_store_dwordx2 v[22:23], v[18:19], off offset:1024
	s_nop 0
	v_mov_b32_e32 v18, 0
	v_mov_b32_e32 v19, 0
	s_nop 0
	s_waitcnt vmcnt(7)
; DI unsigned pk4_fp8(float a, float b, float c, float d) { int w = __builtin_amdgcn_cvt_pk_fp8_f32(sat8(a), sat8(b), 0, false); w = __builtin_amdgcn_cvt_pk_fp8_f32(sat8(c), sat8(d), w, true); return (unsigned)w; }
; template <int l>
; DI void layer_body(LAS unsigned char* lds, const XcdBarrier& bar, const int lo, const int hi, const int G, const int vcu) {
;     ...
;                 for (int r = wave; r < 64; r += 8) { const int dest = dl[r], tk = dl[64 + r];
;                     const u32x4* s = (const u32x4*)(X1B + (size_t)tk * D_); u32x2* d = (u32x2*)((unsigned char*)XS + (size_t)dest * D_);
; #pragma unroll
;                     for (int q = 0; q < 4; ++q) { const u32x4 w = s[lane + 64 * q]; float x[8]; att::unpack8(w, x);
;                         d[lane + 64 * q] = (u32x2){pg8::pk4_fp8(x[0] * X_SC, x[1] * X_SC, x[2] * X_SC, x[3] * X_SC), pg8::pk4_fp8(x[4] * X_SC, x[5] * X_SC, x[6] * X_SC, x[7] * X_SC)}; } }
	v_lshlrev_b32_e32 v1, 16, v236
	v_and_b32_e32 v6, 0xffff0000, v236
	v_lshlrev_b32_e32 v20, 16, v238
	v_and_b32_e32 v8, 0xffff0000, v238
	v_mul_f32_e32 v1, 0x41800000, v1
	v_mul_f32_e32 v6, 0x41800000, v6
	v_mul_f32_e32 v20, 0x41800000, v20
	v_mul_f32_e32 v8, 0x41800000, v8
	v_med3_f32 v1, v1, s44, v16
	v_med3_f32 v6, v6, s44, v16
	v_med3_f32 v20, v20, s44, v16
	v_med3_f32 v8, v8, s44, v16
	v_cvt_pk_fp8_f32 v18, v1, v6
	v_cvt_pk_fp8_f32 v19, v20, v8
	v_lshlrev_b32_e32 v17, 16, v237
	v_and_b32_e32 v7, 0xffff0000, v237
	v_lshlrev_b32_e32 v21, 16, v239
	v_and_b32_e32 v9, 0xffff0000, v239
	v_mul_f32_e32 v17, 0x41800000, v17
	v_mul_f32_e32 v7, 0x41800000, v7
	v_mul_f32_e32 v21, 0x41800000, v21
	v_mul_f32_e32 v9, 0x41800000, v9
	v_med3_f32 v17, v17, s44, v16
	v_med3_f32 v7, v7, s44, v16
	v_med3_f32 v1, v21, s44, v16
	v_med3_f32 v6, v9, s44, v16
	v_cvt_pk_fp8_f32 v18, v17, v7 op_sel:[0,0,1]
	v_cvt_pk_fp8_f32 v19, v1, v6 op_sel:[0,0,1]
	global_store_dwordx2 v[22:23], v[18:19], off offset:1536
	v_mov_b32_e32 v18, 0
	v_mov_b32_e32 v19, 0
	v_ashrrev_i32_e32 v21, 31, v35
	v_mov_b32_e32 v20, v35
	v_ashrrev_i32_e32 v37, 31, v34
	v_mov_b32_e32 v36, v34
	v_lshlrev_b64 v[34:35], 12, v[20:21]
	v_lshlrev_b64 v[36:37], 11, v[36:37]
	v_lshl_add_u64 v[20:21], v[2:3], 0, v[34:35]
	v_lshl_add_u64 v[22:23], v[4:5], 0, v[36:37]
	s_nop 0
	s_cmp_gt_i32 s16, 55
	s_nop 0
	s_waitcnt vmcnt(7)
	v_lshlrev_b32_e32 v1, 16, v232
	v_and_b32_e32 v34, 0xffff0000, v232
	v_lshlrev_b32_e32 v25, 16, v234
	v_and_b32_e32 v36, 0xffff0000, v234
	v_mul_f32_e32 v1, 0x41800000, v1
	v_mul_f32_e32 v34, 0x41800000, v34
	v_mul_f32_e32 v25, 0x41800000, v25
	v_mul_f32_e32 v36, 0x41800000, v36
	v_med3_f32 v1, v1, s44, v16
	v_med3_f32 v34, v34, s44, v16
	v_med3_f32 v25, v25, s44, v16
	v_med3_f32 v36, v36, s44, v16
	v_cvt_pk_fp8_f32 v18, v1, v34
	v_cvt_pk_fp8_f32 v19, v25, v36
	v_lshlrev_b32_e32 v17, 16, v233
	v_and_b32_e32 v35, 0xffff0000, v233
	v_lshlrev_b32_e32 v26, 16, v235
	v_and_b32_e32 v37, 0xffff0000, v235
	v_mul_f32_e32 v17, 0x41800000, v17
	v_mul_f32_e32 v35, 0x41800000, v35
	v_mul_f32_e32 v26, 0x41800000, v26
	v_mul_f32_e32 v37, 0x41800000, v37
	v_med3_f32 v17, v17, s44, v16
	v_med3_f32 v35, v35, s44, v16
	v_med3_f32 v26, v26, s44, v16
	v_med3_f32 v37, v37, s44, v16
	v_cvt_pk_fp8_f32 v18, v17, v35 op_sel:[0,0,1]
	v_cvt_pk_fp8_f32 v19, v26, v37 op_sel:[0,0,1]
	global_store_dwordx2 v[22:23], v[18:19], off
	s_nop 0
	v_mov_b32_e32 v18, 0
	v_mov_b32_e32 v19, 0
	s_nop 0
	s_waitcnt vmcnt(7)
	v_lshlrev_b32_e32 v1, 16, v228
	v_and_b32_e32 v34, 0xffff0000, v228
	v_lshlrev_b32_e32 v25, 16, v230
	v_and_b32_e32 v36, 0xffff0000, v230
	v_mul_f32_e32 v1, 0x41800000, v1
	v_mul_f32_e32 v34, 0x41800000, v34
	v_mul_f32_e32 v25, 0x41800000, v25
	v_mul_f32_e32 v36, 0x41800000, v36
	v_med3_f32 v1, v1, s44, v16
	v_med3_f32 v34, v34, s44, v16
	v_med3_f32 v25, v25, s44, v16
	v_med3_f32 v36, v36, s44, v16
	v_cvt_pk_fp8_f32 v18, v1, v34
	v_cvt_pk_fp8_f32 v19, v25, v36
	v_lshlrev_b32_e32 v17, 16, v229
	v_and_b32_e32 v35, 0xffff0000, v229
	v_lshlrev_b32_e32 v26, 16, v231
	v_and_b32_e32 v37, 0xffff0000, v231
	v_mul_f32_e32 v17, 0x41800000, v17
	v_mul_f32_e32 v35, 0x41800000, v35
	v_mul_f32_e32 v26, 0x41800000, v26
	v_mul_f32_e32 v37, 0x41800000, v37
	v_med3_f32 v17, v17, s44, v16
	v_med3_f32 v35, v35, s44, v16
	v_med3_f32 v26, v26, s44, v16
	v_med3_f32 v37, v37, s44, v16
	v_cvt_pk_fp8_f32 v18, v17, v35 op_sel:[0,0,1]
	v_cvt_pk_fp8_f32 v19, v26, v37 op_sel:[0,0,1]
	global_store_dwordx2 v[22:23], v[18:19], off offset:512
	s_nop 0
	v_mov_b32_e32 v18, 0
	v_mov_b32_e32 v19, 0
	s_nop 0
	s_waitcnt vmcnt(7)
	v_lshlrev_b32_e32 v1, 16, v224
	v_and_b32_e32 v34, 0xffff0000, v224
	v_lshlrev_b32_e32 v25, 16, v226
	v_and_b32_e32 v36, 0xffff0000, v226
	v_mul_f32_e32 v1, 0x41800000, v1
	v_mul_f32_e32 v34, 0x41800000, v34
	v_mul_f32_e32 v25, 0x41800000, v25
	v_mul_f32_e32 v36, 0x41800000, v36
	v_med3_f32 v1, v1, s44, v16
	v_med3_f32 v34, v34, s44, v16
	v_med3_f32 v25, v25, s44, v16
	v_med3_f32 v36, v36, s44, v16
	v_cvt_pk_fp8_f32 v18, v1, v34
	v_cvt_pk_fp8_f32 v19, v25, v36
	v_lshlrev_b32_e32 v17, 16, v225
	v_and_b32_e32 v35, 0xffff0000, v225
	v_lshlrev_b32_e32 v26, 16, v227
	v_and_b32_e32 v37, 0xffff0000, v227
	v_mul_f32_e32 v17, 0x41800000, v17
	v_mul_f32_e32 v35, 0x41800000, v35
	v_mul_f32_e32 v26, 0x41800000, v26
	v_mul_f32_e32 v37, 0x41800000, v37
	v_med3_f32 v17, v17, s44, v16
	v_med3_f32 v35, v35, s44, v16
	v_med3_f32 v26, v26, s44, v16
	v_med3_f32 v37, v37, s44, v16
	v_cvt_pk_fp8_f32 v18, v17, v35 op_sel:[0,0,1]
	v_cvt_pk_fp8_f32 v19, v26, v37 op_sel:[0,0,1]
	global_store_dwordx2 v[22:23], v[18:19], off offset:1024
	s_nop 0
	v_mov_b32_e32 v18, 0
	v_mov_b32_e32 v19, 0
	s_nop 0
	s_waitcnt vmcnt(7)
	v_lshlrev_b32_e32 v1, 16, v220
	v_and_b32_e32 v34, 0xffff0000, v220
	v_lshlrev_b32_e32 v20, 16, v222
	v_and_b32_e32 v36, 0xffff0000, v222
	v_mul_f32_e32 v1, 0x41800000, v1
	v_mul_f32_e32 v34, 0x41800000, v34
	v_mul_f32_e32 v20, 0x41800000, v20
	v_mul_f32_e32 v36, 0x41800000, v36
	v_med3_f32 v1, v1, s44, v16
	v_med3_f32 v34, v34, s44, v16
	v_med3_f32 v20, v20, s44, v16
	v_med3_f32 v36, v36, s44, v16
	v_cvt_pk_fp8_f32 v18, v1, v34
	v_cvt_pk_fp8_f32 v19, v20, v36
	v_lshlrev_b32_e32 v17, 16, v221
	v_and_b32_e32 v35, 0xffff0000, v221
	v_lshlrev_b32_e32 v21, 16, v223
	v_and_b32_e32 v37, 0xffff0000, v223
	v_mul_f32_e32 v17, 0x41800000, v17
	v_mul_f32_e32 v35, 0x41800000, v35
	v_mul_f32_e32 v21, 0x41800000, v21
	v_mul_f32_e32 v37, 0x41800000, v37
	v_med3_f32 v17, v17, s44, v16
	v_med3_f32 v35, v35, s44, v16
	v_med3_f32 v1, v21, s44, v16
	v_med3_f32 v34, v37, s44, v16
	v_cvt_pk_fp8_f32 v18, v17, v35 op_sel:[0,0,1]
	v_cvt_pk_fp8_f32 v19, v1, v34 op_sel:[0,0,1]
	global_store_dwordx2 v[22:23], v[18:19], off offset:1536
	s_cbranch_scc0 .LBB0_1539
	s_branch .LBB0_1519
